# speedup vs baseline: 1.0420x; 1.0001x over previous
.LBB2_73:
	s_add_u32 s6, s0, 48
	s_addc_u32 s7, s1, 0
	s_load_dwordx8 s[24:31], s[6:7], 0x234
	s_load_dword s32, s[6:7], 0x254
	s_ashr_i32 s8, s2, 2
	s_mov_b64 s[0:1], 0
	s_waitcnt lgkmcnt(0)
	s_cmp_ge_i32 s8, s24
	s_addc_u32 s0, s0, 0
	s_cmp_ge_i32 s8, s25
	s_addc_u32 s0, s0, 0
	s_cmp_ge_i32 s8, s26
	s_addc_u32 s0, s0, 0
	s_cmp_ge_i32 s8, s27
	s_addc_u32 s0, s0, 0
	s_cmp_ge_i32 s8, s28
	s_addc_u32 s0, s0, 0
	s_cmp_ge_i32 s8, s29
	s_addc_u32 s0, s0, 0
	s_cmp_ge_i32 s8, s30
	s_addc_u32 s0, s0, 0
	s_cmp_ge_i32 s8, s31
	s_addc_u32 s0, s0, 0
	s_cmp_ge_i32 s8, s32
	s_addc_u32 s0, s0, 0
